# GEMM2 K-loop: the leading wave half runs its own loop copy whose counted DMA waits sit after each phase's MFMAs (one more barrier interval of flight time for its pieces), on top of v34
# speedup vs baseline: 1.0051x; 1.0051x over previous
.LBB0_2088:
	ds_read_b128 v[18:21], v180
	ds_read_b128 v[22:25], v181
	ds_read_b128 v[26:29], v182
	ds_read_b128 v[30:33], v183
	ds_read_b128 v[2:5], v184
	ds_read_b128 v[6:9], v185
	ds_read_b128 v[10:13], v186
	ds_read_b128 v[14:17], v187
	s_ashr_i32 s13, s12, 31
	s_lshl_b64 s[38:39], s[12:13], 18
	s_add_u32 s38, s53, s38
	s_addc_u32 s39, s54, s39
	s_and_b64 s[46:47], s[48:49], exec
	s_cselect_b32 s13, s39, s43
	s_cselect_b32 s27, s38, s42
	s_add_u32 s46, s42, 0x20080
	s_addc_u32 s47, s43, 0
	s_add_i32 s29, s37, 0xc000
	v_lshl_add_u64 v[224:225], s[46:47], 0, v[162:163]
	s_mov_b32 m0, s29
	s_add_i32 s31, s37, 0xe000
	ds_read_b128 v[172:175], v196
	ds_read_b128 v[176:179], v196 offset:1024
	ds_read_b128 v[198:201], v196 offset:2048
	ds_read_b128 v[202:205], v196 offset:3072
	ds_read_b128 v[206:209], v196 offset:4096
	ds_read_b128 v[210:213], v196 offset:5120
	ds_read_b128 v[216:219], v196 offset:6144
	ds_read_b128 v[220:223], v196 offset:7168
	global_load_lds_dwordx4 v[224:225], off
	v_lshl_add_u64 v[224:225], s[46:47], 0, v[164:165]
	s_mov_b32 m0, s31
	s_nop 0
	global_load_lds_dwordx4 v[224:225], off
	s_cmp_lg_u64 s[8:9], 0
	s_cbranch_scc1 .Lg2l_start
	s_cmp_eq_u32 s26, 0
	s_cbranch_scc1 .Lrw_first_g2_0
	s_waitcnt vmcnt(24)
	s_branch .Lrw_done_g2_0

.LBB0_2089:
	ds_read_b128 v[2:5], v180
	ds_read_b128 v[6:9], v181
	ds_read_b128 v[10:13], v182
	ds_read_b128 v[14:17], v183
	ds_read_b128 v[26:29], v184
	ds_read_b128 v[30:33], v185
	ds_read_b128 v[172:175], v186
	ds_read_b128 v[176:179], v187
	s_add_u32 s44, s42, 0xfffe0080
	s_addc_u32 s45, s43, -1
	s_cmp_eq_u32 s74, 4
	s_cselect_b32 s47, s13, s45
	s_cselect_b32 s46, s27, s44
	s_cselect_b32 s45, s35, s49
	s_cselect_b32 s44, s34, s48
	s_mov_b32 m0, s29
	v_lshl_add_u64 v[224:225], s[42:43], 0, v[168:169]
	ds_read_b128 v[18:21], v196
	ds_read_b128 v[22:25], v196 offset:1024
	ds_read_b128 v[198:201], v196 offset:2048
	ds_read_b128 v[202:205], v196 offset:3072
	ds_read_b128 v[206:209], v196 offset:4096
	ds_read_b128 v[210:213], v196 offset:5120
	ds_read_b128 v[216:219], v196 offset:6144
	ds_read_b128 v[220:223], v196 offset:7168
	global_load_lds_dwordx4 v[224:225], off
	v_lshl_add_u64 v[224:225], s[42:43], 0, v[170:171]
	s_mov_b32 m0, s31
	s_nop 0
	global_load_lds_dwordx4 v[224:225], off
	s_waitcnt vmcnt(8)
	s_waitcnt lgkmcnt(0)
	s_barrier
	s_setprio 1
	s_waitcnt lgkmcnt(0)
	v_mfma_scale_f32_16x16x128_f8f6f4 v[158:161], v[2:9], v[18:25], v[158:161], v234, v238 op_sel_hi:[0,0,0]
	v_mfma_scale_f32_16x16x128_f8f6f4 v[154:157], v[10:17], v[18:25], v[154:157], v234, v238 op_sel_hi:[0,0,0]
	v_mfma_scale_f32_16x16x128_f8f6f4 v[150:153], v[2:9], v[198:205], v[150:153], v234, v238 op_sel_hi:[0,0,0]
	v_mfma_scale_f32_16x16x128_f8f6f4 v[146:149], v[10:17], v[198:205], v[146:149], v234, v238 op_sel_hi:[0,0,0]
	v_mfma_scale_f32_16x16x128_f8f6f4 v[142:145], v[2:9], v[206:213], v[142:145], v234, v238 op_sel_hi:[0,0,0]
	v_mfma_scale_f32_16x16x128_f8f6f4 v[138:141], v[10:17], v[206:213], v[138:141], v234, v238 op_sel_hi:[0,0,0]
	v_mfma_scale_f32_16x16x128_f8f6f4 v[134:137], v[2:9], v[216:223], v[134:137], v234, v238 op_sel_hi:[0,0,0]
	v_mfma_scale_f32_16x16x128_f8f6f4 v[130:133], v[10:17], v[216:223], v[130:133], v234, v238 op_sel_hi:[0,0,0]
	s_setprio 0
	s_setprio 1
	v_mfma_scale_f32_16x16x128_f8f6f4 v[126:129], v[26:33], v[18:25], v[126:129], v234, v238 op_sel_hi:[0,0,0]
	v_mfma_scale_f32_16x16x128_f8f6f4 v[122:125], v[172:179], v[18:25], v[122:125], v234, v238 op_sel_hi:[0,0,0]
	v_mfma_scale_f32_16x16x128_f8f6f4 v[118:121], v[26:33], v[198:205], v[118:121], v234, v238 op_sel_hi:[0,0,0]
	v_mfma_scale_f32_16x16x128_f8f6f4 v[114:117], v[172:179], v[198:205], v[114:117], v234, v238 op_sel_hi:[0,0,0]
	v_mfma_scale_f32_16x16x128_f8f6f4 v[110:113], v[26:33], v[206:213], v[110:113], v234, v238 op_sel_hi:[0,0,0]
	v_mfma_scale_f32_16x16x128_f8f6f4 v[106:109], v[172:179], v[206:213], v[106:109], v234, v238 op_sel_hi:[0,0,0]
	v_mfma_scale_f32_16x16x128_f8f6f4 v[102:105], v[26:33], v[216:223], v[102:105], v234, v238 op_sel_hi:[0,0,0]
	v_mfma_scale_f32_16x16x128_f8f6f4 v[98:101], v[172:179], v[216:223], v[98:101], v234, v238 op_sel_hi:[0,0,0]
	s_setprio 0
	s_barrier
	s_mov_b32 m0, s41
	v_lshl_add_u64 v[18:19], s[44:45], 0, v[0:1]
	s_add_u32 vcc_lo, s44, 0x20000
	ds_read_b128 v[198:201], v196 offset:16384
	ds_read_b128 v[202:205], v196 offset:17408
	ds_read_b128 v[206:209], v196 offset:18432
	ds_read_b128 v[210:213], v196 offset:19456
	ds_read_b128 v[216:219], v196 offset:20480
	ds_read_b128 v[220:223], v196 offset:21504
	ds_read_b128 v[224:227], v196 offset:22528
	ds_read_b128 v[228:231], v196 offset:23552
	global_load_lds_dwordx4 v[18:19], off
	v_lshl_add_u64 v[20:21], s[44:45], 0, v[166:167]
	s_mov_b32 m0, s57
	s_addc_u32 vcc_hi, s45, 0
	global_load_lds_dwordx4 v[20:21], off
	v_lshl_add_u64 v[22:23], vcc, 0, v[0:1]
	s_mov_b32 m0, s58
	v_lshl_add_u64 v[24:25], s[46:47], 0, v[164:165]
	global_load_lds_dwordx4 v[22:23], off
	v_lshl_add_u64 v[22:23], vcc, 0, v[166:167]
	s_mov_b32 m0, s59
	s_nop 0
	global_load_lds_dwordx4 v[22:23], off
	v_lshl_add_u64 v[22:23], s[46:47], 0, v[162:163]
	s_mov_b32 m0, s37
	s_nop 0
	global_load_lds_dwordx4 v[22:23], off
	s_mov_b32 m0, s60
	s_nop 0
	global_load_lds_dwordx4 v[24:25], off
	s_waitcnt vmcnt(8)
	s_waitcnt lgkmcnt(0)
	s_barrier
	s_setprio 1
	s_waitcnt lgkmcnt(0)
	v_mfma_scale_f32_16x16x128_f8f6f4 v[94:97], v[2:9], v[198:205], v[94:97], v234, v238 op_sel_hi:[0,0,0]
	v_mfma_scale_f32_16x16x128_f8f6f4 v[90:93], v[10:17], v[198:205], v[90:93], v234, v238 op_sel_hi:[0,0,0]
	v_mfma_scale_f32_16x16x128_f8f6f4 v[86:89], v[2:9], v[206:213], v[86:89], v234, v238 op_sel_hi:[0,0,0]
	v_mfma_scale_f32_16x16x128_f8f6f4 v[82:85], v[10:17], v[206:213], v[82:85], v234, v238 op_sel_hi:[0,0,0]
	v_mfma_scale_f32_16x16x128_f8f6f4 v[78:81], v[2:9], v[216:223], v[78:81], v234, v238 op_sel_hi:[0,0,0]
	v_mfma_scale_f32_16x16x128_f8f6f4 v[74:77], v[10:17], v[216:223], v[74:77], v234, v238 op_sel_hi:[0,0,0]
	v_mfma_scale_f32_16x16x128_f8f6f4 v[70:73], v[2:9], v[224:231], v[70:73], v234, v238 op_sel_hi:[0,0,0]
	v_mfma_scale_f32_16x16x128_f8f6f4 v[66:69], v[10:17], v[224:231], v[66:69], v234, v238 op_sel_hi:[0,0,0]
	s_setprio 0
	s_setprio 1
	v_mfma_scale_f32_16x16x128_f8f6f4 v[62:65], v[26:33], v[198:205], v[62:65], v234, v238 op_sel_hi:[0,0,0]
	v_mfma_scale_f32_16x16x128_f8f6f4 v[58:61], v[172:179], v[198:205], v[58:61], v234, v238 op_sel_hi:[0,0,0]
	v_mfma_scale_f32_16x16x128_f8f6f4 v[54:57], v[26:33], v[206:213], v[54:57], v234, v238 op_sel_hi:[0,0,0]
	v_mfma_scale_f32_16x16x128_f8f6f4 v[50:53], v[172:179], v[206:213], v[50:53], v234, v238 op_sel_hi:[0,0,0]
	v_mfma_scale_f32_16x16x128_f8f6f4 v[46:49], v[26:33], v[216:223], v[46:49], v234, v238 op_sel_hi:[0,0,0]
	v_mfma_scale_f32_16x16x128_f8f6f4 v[42:45], v[172:179], v[216:223], v[42:45], v234, v238 op_sel_hi:[0,0,0]
	v_mfma_scale_f32_16x16x128_f8f6f4 v[38:41], v[26:33], v[224:231], v[38:41], v234, v238 op_sel_hi:[0,0,0]
	v_mfma_scale_f32_16x16x128_f8f6f4 v[34:37], v[172:179], v[224:231], v[34:37], v234, v238 op_sel_hi:[0,0,0]
	s_setprio 0
	s_barrier
	ds_read_b128 v[10:13], v188
	ds_read_b128 v[14:17], v189
	ds_read_b128 v[26:29], v190
	ds_read_b128 v[30:33], v191
	ds_read_b128 v[2:5], v192
	ds_read_b128 v[6:9], v193
	ds_read_b128 v[172:175], v194
	ds_read_b128 v[176:179], v195
	s_add_u32 s46, s46, 0x20000
	s_addc_u32 s47, s47, 0
	s_mov_b32 m0, s61
	v_lshl_add_u64 v[232:233], s[46:47], 0, v[162:163]
	ds_read_b128 v[198:201], v196 offset:32768
	ds_read_b128 v[202:205], v196 offset:33792
	ds_read_b128 v[206:209], v196 offset:34816
	ds_read_b128 v[210:213], v196 offset:35840
	ds_read_b128 v[216:219], v196 offset:36864
	ds_read_b128 v[220:223], v196 offset:37888
	ds_read_b128 v[224:227], v196 offset:38912
	ds_read_b128 v[228:231], v196 offset:39936
	global_load_lds_dwordx4 v[232:233], off
	v_lshl_add_u64 v[232:233], s[46:47], 0, v[164:165]
	s_mov_b32 m0, s62
	s_nop 0
	global_load_lds_dwordx4 v[232:233], off
	s_waitcnt vmcnt(8)
	s_waitcnt lgkmcnt(0)
	s_barrier
	s_setprio 1
	s_waitcnt lgkmcnt(0)
	v_mfma_scale_f32_16x16x128_f8f6f4 v[158:161], v[10:17], v[198:205], v[158:161], v234, v238 op_sel_hi:[0,0,0]
	v_mfma_scale_f32_16x16x128_f8f6f4 v[154:157], v[26:33], v[198:205], v[154:157], v234, v238 op_sel_hi:[0,0,0]
	v_mfma_scale_f32_16x16x128_f8f6f4 v[150:153], v[10:17], v[206:213], v[150:153], v234, v238 op_sel_hi:[0,0,0]
	v_mfma_scale_f32_16x16x128_f8f6f4 v[146:149], v[26:33], v[206:213], v[146:149], v234, v238 op_sel_hi:[0,0,0]
	v_mfma_scale_f32_16x16x128_f8f6f4 v[142:145], v[10:17], v[216:223], v[142:145], v234, v238 op_sel_hi:[0,0,0]
	v_mfma_scale_f32_16x16x128_f8f6f4 v[138:141], v[26:33], v[216:223], v[138:141], v234, v238 op_sel_hi:[0,0,0]
	v_mfma_scale_f32_16x16x128_f8f6f4 v[134:137], v[10:17], v[224:231], v[134:137], v234, v238 op_sel_hi:[0,0,0]
	v_mfma_scale_f32_16x16x128_f8f6f4 v[130:133], v[26:33], v[224:231], v[130:133], v234, v238 op_sel_hi:[0,0,0]
	s_setprio 0
	s_setprio 1
	v_mfma_scale_f32_16x16x128_f8f6f4 v[126:129], v[2:9], v[198:205], v[126:129], v234, v238 op_sel_hi:[0,0,0]
	v_mfma_scale_f32_16x16x128_f8f6f4 v[122:125], v[172:179], v[198:205], v[122:125], v234, v238 op_sel_hi:[0,0,0]
	v_mfma_scale_f32_16x16x128_f8f6f4 v[118:121], v[2:9], v[206:213], v[118:121], v234, v238 op_sel_hi:[0,0,0]
	v_mfma_scale_f32_16x16x128_f8f6f4 v[114:117], v[172:179], v[206:213], v[114:117], v234, v238 op_sel_hi:[0,0,0]
	v_mfma_scale_f32_16x16x128_f8f6f4 v[110:113], v[2:9], v[216:223], v[110:113], v234, v238 op_sel_hi:[0,0,0]
	v_mfma_scale_f32_16x16x128_f8f6f4 v[106:109], v[172:179], v[216:223], v[106:109], v234, v238 op_sel_hi:[0,0,0]
	v_mfma_scale_f32_16x16x128_f8f6f4 v[102:105], v[2:9], v[224:231], v[102:105], v234, v238 op_sel_hi:[0,0,0]
	v_mfma_scale_f32_16x16x128_f8f6f4 v[98:101], v[172:179], v[224:231], v[98:101], v234, v238 op_sel_hi:[0,0,0]
	s_setprio 0
	s_barrier
	s_mov_b32 m0, s65
	v_lshl_add_u64 v[18:19], v[18:19], 0, s[66:67]
	s_add_u32 s44, s44, 0x20080
	ds_read_b128 v[198:201], v196 offset:49152
	ds_read_b128 v[202:205], v196 offset:50176
	ds_read_b128 v[206:209], v196 offset:51200
	ds_read_b128 v[210:213], v196 offset:52224
	ds_read_b128 v[216:219], v196 offset:53248
	ds_read_b128 v[220:223], v196 offset:54272
	ds_read_b128 v[224:227], v196 offset:55296
	ds_read_b128 v[228:231], v196 offset:56320
	global_load_lds_dwordx4 v[18:19], off
	v_lshl_add_u64 v[18:19], v[20:21], 0, s[66:67]
	s_mov_b32 m0, s68
	s_addc_u32 s45, s45, 0
	global_load_lds_dwordx4 v[18:19], off
	v_lshl_add_u64 v[18:19], s[44:45], 0, v[0:1]
	s_mov_b32 m0, s51
	s_nop 0
	global_load_lds_dwordx4 v[18:19], off
	v_lshl_add_u64 v[18:19], s[44:45], 0, v[166:167]
	s_mov_b32 m0, s4
	s_nop 0
	global_load_lds_dwordx4 v[18:19], off
	v_lshl_add_u64 v[18:19], v[22:23], 0, s[66:67]
	s_mov_b32 m0, s81
	s_nop 0
	global_load_lds_dwordx4 v[18:19], off
	v_lshl_add_u64 v[18:19], v[24:25], 0, s[66:67]
	s_mov_b32 m0, s50
	s_nop 0
	global_load_lds_dwordx4 v[18:19], off
	s_waitcnt vmcnt(8)
	s_waitcnt lgkmcnt(0)
	s_barrier
	s_setprio 1
	s_waitcnt lgkmcnt(0)
	v_mfma_scale_f32_16x16x128_f8f6f4 v[94:97], v[10:17], v[198:205], v[94:97], v234, v238 op_sel_hi:[0,0,0]
	v_mfma_scale_f32_16x16x128_f8f6f4 v[90:93], v[26:33], v[198:205], v[90:93], v234, v238 op_sel_hi:[0,0,0]
	v_mfma_scale_f32_16x16x128_f8f6f4 v[86:89], v[10:17], v[206:213], v[86:89], v234, v238 op_sel_hi:[0,0,0]
	v_mfma_scale_f32_16x16x128_f8f6f4 v[82:85], v[26:33], v[206:213], v[82:85], v234, v238 op_sel_hi:[0,0,0]
	v_mfma_scale_f32_16x16x128_f8f6f4 v[78:81], v[10:17], v[216:223], v[78:81], v234, v238 op_sel_hi:[0,0,0]
	v_mfma_scale_f32_16x16x128_f8f6f4 v[74:77], v[26:33], v[216:223], v[74:77], v234, v238 op_sel_hi:[0,0,0]
	v_mfma_scale_f32_16x16x128_f8f6f4 v[70:73], v[10:17], v[224:231], v[70:73], v234, v238 op_sel_hi:[0,0,0]
	v_mfma_scale_f32_16x16x128_f8f6f4 v[66:69], v[26:33], v[224:231], v[66:69], v234, v238 op_sel_hi:[0,0,0]
	s_setprio 0
	s_setprio 1
	v_mfma_scale_f32_16x16x128_f8f6f4 v[62:65], v[2:9], v[198:205], v[62:65], v234, v238 op_sel_hi:[0,0,0]
	v_mfma_scale_f32_16x16x128_f8f6f4 v[58:61], v[172:179], v[198:205], v[58:61], v234, v238 op_sel_hi:[0,0,0]
	v_mfma_scale_f32_16x16x128_f8f6f4 v[54:57], v[2:9], v[206:213], v[54:57], v234, v238 op_sel_hi:[0,0,0]
	v_mfma_scale_f32_16x16x128_f8f6f4 v[50:53], v[172:179], v[206:213], v[50:53], v234, v238 op_sel_hi:[0,0,0]
	v_mfma_scale_f32_16x16x128_f8f6f4 v[46:49], v[2:9], v[216:223], v[46:49], v234, v238 op_sel_hi:[0,0,0]
	v_mfma_scale_f32_16x16x128_f8f6f4 v[42:45], v[172:179], v[216:223], v[42:45], v234, v238 op_sel_hi:[0,0,0]
	v_mfma_scale_f32_16x16x128_f8f6f4 v[38:41], v[2:9], v[224:231], v[38:41], v234, v238 op_sel_hi:[0,0,0]
	v_mfma_scale_f32_16x16x128_f8f6f4 v[34:37], v[172:179], v[224:231], v[34:37], v234, v238 op_sel_hi:[0,0,0]
	s_setprio 0
	s_barrier
	s_add_i32 s74, s74, 2
	s_add_u32 s42, s42, 0x100
	s_addc_u32 s43, s43, 0
	s_add_u32 s48, s48, 0x100
	s_addc_u32 s49, s49, 0
	s_cmp_gt_u32 s74, 5
	s_cbranch_scc0 .LBB0_2089
	s_branch .Lg2_join
.Lg2l_start:
	s_waitcnt lgkmcnt(0)
	s_barrier
	s_setprio 1
	s_waitcnt lgkmcnt(0)
	v_mfma_scale_f32_16x16x128_f8f6f4 v[158:161], v[18:25], v[172:179], 0, v234, v238 op_sel_hi:[0,0,0]
	v_mfma_scale_f32_16x16x128_f8f6f4 v[154:157], v[26:33], v[172:179], 0, v234, v238 op_sel_hi:[0,0,0]
	v_mfma_scale_f32_16x16x128_f8f6f4 v[150:153], v[18:25], v[198:205], 0, v234, v238 op_sel_hi:[0,0,0]
	v_mfma_scale_f32_16x16x128_f8f6f4 v[146:149], v[26:33], v[198:205], 0, v234, v238 op_sel_hi:[0,0,0]
	v_mfma_scale_f32_16x16x128_f8f6f4 v[142:145], v[18:25], v[206:213], 0, v234, v238 op_sel_hi:[0,0,0]
	v_mfma_scale_f32_16x16x128_f8f6f4 v[138:141], v[26:33], v[206:213], 0, v234, v238 op_sel_hi:[0,0,0]
	v_mfma_scale_f32_16x16x128_f8f6f4 v[134:137], v[18:25], v[216:223], 0, v234, v238 op_sel_hi:[0,0,0]
	v_mfma_scale_f32_16x16x128_f8f6f4 v[130:133], v[26:33], v[216:223], 0, v234, v238 op_sel_hi:[0,0,0]
	s_setprio 0
	s_setprio 1
	v_mfma_scale_f32_16x16x128_f8f6f4 v[126:129], v[2:9], v[172:179], 0, v234, v238 op_sel_hi:[0,0,0]
	v_mfma_scale_f32_16x16x128_f8f6f4 v[122:125], v[10:17], v[172:179], 0, v234, v238 op_sel_hi:[0,0,0]
	v_mfma_scale_f32_16x16x128_f8f6f4 v[118:121], v[2:9], v[198:205], 0, v234, v238 op_sel_hi:[0,0,0]
	v_mfma_scale_f32_16x16x128_f8f6f4 v[114:117], v[10:17], v[198:205], 0, v234, v238 op_sel_hi:[0,0,0]
	v_mfma_scale_f32_16x16x128_f8f6f4 v[110:113], v[2:9], v[206:213], 0, v234, v238 op_sel_hi:[0,0,0]
	v_mfma_scale_f32_16x16x128_f8f6f4 v[106:109], v[10:17], v[206:213], 0, v234, v238 op_sel_hi:[0,0,0]
	v_mfma_scale_f32_16x16x128_f8f6f4 v[102:105], v[2:9], v[216:223], 0, v234, v238 op_sel_hi:[0,0,0]
	v_mfma_scale_f32_16x16x128_f8f6f4 v[98:101], v[10:17], v[216:223], 0, v234, v238 op_sel_hi:[0,0,0]
	s_setprio 0
	s_cmp_eq_u32 s26, 0
	s_cbranch_scc1 .Lg2l_rw_first_g2_0
	s_waitcnt vmcnt(24)
	s_branch .Lg2l_rw_done_g2_0

.Lg2l_rw_done_g2_0:
	s_barrier
	v_lshl_add_u64 v[172:173], s[44:45], 0, v[0:1]
	s_mov_b64 s[48:49], 0x100
	s_mov_b32 m0, s41
	v_lshl_add_u64 v[174:175], v[172:173], 0, s[48:49]
	ds_read_b128 v[198:201], v196 offset:16384
	ds_read_b128 v[202:205], v196 offset:17408
	ds_read_b128 v[206:209], v196 offset:18432
	ds_read_b128 v[210:213], v196 offset:19456
	ds_read_b128 v[216:219], v196 offset:20480
	ds_read_b128 v[220:223], v196 offset:21504
	ds_read_b128 v[224:227], v196 offset:22528
	ds_read_b128 v[228:231], v196 offset:23552
	global_load_lds_dwordx4 v[174:175], off
	v_lshl_add_u64 v[174:175], s[44:45], 0, v[166:167]
	s_add_u32 s46, s44, 0x20100
	v_lshl_add_u64 v[176:177], v[174:175], 0, s[48:49]
	s_mov_b32 m0, s57
	s_addc_u32 s47, s45, 0
	global_load_lds_dwordx4 v[176:177], off
	v_lshl_add_u64 v[176:177], s[46:47], 0, v[0:1]
	s_mov_b32 m0, s58
	s_nop 0
	global_load_lds_dwordx4 v[176:177], off
	v_lshl_add_u64 v[176:177], s[46:47], 0, v[166:167]
	s_mov_b32 m0, s59
	s_nop 0
	global_load_lds_dwordx4 v[176:177], off
	v_lshl_add_u64 v[176:177], s[42:43], 0, v[162:163]
	v_lshl_add_u64 v[178:179], v[176:177], 0, s[48:49]
	s_mov_b32 m0, s37
	s_nop 0
	global_load_lds_dwordx4 v[178:179], off
	v_lshl_add_u64 v[178:179], s[42:43], 0, v[164:165]
	v_lshl_add_u64 v[232:233], v[178:179], 0, s[48:49]
	s_mov_b32 m0, s60
	s_nop 0
	global_load_lds_dwordx4 v[232:233], off
	s_waitcnt lgkmcnt(0)
	s_barrier
	s_setprio 1
	s_waitcnt lgkmcnt(0)
	v_mfma_scale_f32_16x16x128_f8f6f4 v[94:97], v[18:25], v[198:205], 0, v234, v238 op_sel_hi:[0,0,0]
	v_mfma_scale_f32_16x16x128_f8f6f4 v[90:93], v[26:33], v[198:205], 0, v234, v238 op_sel_hi:[0,0,0]
	v_mfma_scale_f32_16x16x128_f8f6f4 v[86:89], v[18:25], v[206:213], 0, v234, v238 op_sel_hi:[0,0,0]
	v_mfma_scale_f32_16x16x128_f8f6f4 v[82:85], v[26:33], v[206:213], 0, v234, v238 op_sel_hi:[0,0,0]
	v_mfma_scale_f32_16x16x128_f8f6f4 v[78:81], v[18:25], v[216:223], 0, v234, v238 op_sel_hi:[0,0,0]
	v_mfma_scale_f32_16x16x128_f8f6f4 v[74:77], v[26:33], v[216:223], 0, v234, v238 op_sel_hi:[0,0,0]
	v_mfma_scale_f32_16x16x128_f8f6f4 v[70:73], v[18:25], v[224:231], 0, v234, v238 op_sel_hi:[0,0,0]
	v_mfma_scale_f32_16x16x128_f8f6f4 v[66:69], v[26:33], v[224:231], 0, v234, v238 op_sel_hi:[0,0,0]
	s_setprio 0
	s_setprio 1
	v_mfma_scale_f32_16x16x128_f8f6f4 v[62:65], v[2:9], v[198:205], 0, v234, v238 op_sel_hi:[0,0,0]
	v_mfma_scale_f32_16x16x128_f8f6f4 v[58:61], v[10:17], v[198:205], 0, v234, v238 op_sel_hi:[0,0,0]
	v_mfma_scale_f32_16x16x128_f8f6f4 v[54:57], v[2:9], v[206:213], 0, v234, v238 op_sel_hi:[0,0,0]
	v_mfma_scale_f32_16x16x128_f8f6f4 v[50:53], v[10:17], v[206:213], 0, v234, v238 op_sel_hi:[0,0,0]
	v_mfma_scale_f32_16x16x128_f8f6f4 v[46:49], v[2:9], v[216:223], 0, v234, v238 op_sel_hi:[0,0,0]
	v_mfma_scale_f32_16x16x128_f8f6f4 v[42:45], v[10:17], v[216:223], 0, v234, v238 op_sel_hi:[0,0,0]
	v_mfma_scale_f32_16x16x128_f8f6f4 v[38:41], v[2:9], v[224:231], 0, v234, v238 op_sel_hi:[0,0,0]
	v_mfma_scale_f32_16x16x128_f8f6f4 v[34:37], v[10:17], v[224:231], 0, v234, v238 op_sel_hi:[0,0,0]
	s_setprio 0
	s_cmp_eq_u32 s26, 0
	s_cbranch_scc1 .Lg2l_rw_first_g2_1
	s_waitcnt vmcnt(24)
	s_branch .Lg2l_rw_done_g2_1

.Lg2l_rw_done_g2_1:
	s_barrier
	ds_read_b128 v[18:21], v188
	ds_read_b128 v[22:25], v189
	ds_read_b128 v[26:29], v190
	ds_read_b128 v[30:33], v191
	ds_read_b128 v[2:5], v192
	ds_read_b128 v[6:9], v193
	ds_read_b128 v[10:13], v194
	ds_read_b128 v[14:17], v195
	s_add_u32 s46, s42, 0x20100
	s_addc_u32 s47, s43, 0
	s_mov_b32 m0, s61
	v_lshl_add_u64 v[232:233], s[46:47], 0, v[162:163]
	ds_read_b128 v[198:201], v196 offset:32768
	ds_read_b128 v[202:205], v196 offset:33792
	ds_read_b128 v[206:209], v196 offset:34816
	ds_read_b128 v[210:213], v196 offset:35840
	ds_read_b128 v[216:219], v196 offset:36864
	ds_read_b128 v[220:223], v196 offset:37888
	ds_read_b128 v[224:227], v196 offset:38912
	ds_read_b128 v[228:231], v196 offset:39936
	global_load_lds_dwordx4 v[232:233], off
	v_lshl_add_u64 v[232:233], s[46:47], 0, v[164:165]
	s_mov_b32 m0, s62
	s_nop 0
	global_load_lds_dwordx4 v[232:233], off
	s_waitcnt lgkmcnt(0)
	s_barrier
	s_setprio 1
	s_waitcnt lgkmcnt(0)
	v_mfma_scale_f32_16x16x128_f8f6f4 v[158:161], v[18:25], v[198:205], v[158:161], v234, v238 op_sel_hi:[0,0,0]
	v_mfma_scale_f32_16x16x128_f8f6f4 v[154:157], v[26:33], v[198:205], v[154:157], v234, v238 op_sel_hi:[0,0,0]
	v_mfma_scale_f32_16x16x128_f8f6f4 v[150:153], v[18:25], v[206:213], v[150:153], v234, v238 op_sel_hi:[0,0,0]
	v_mfma_scale_f32_16x16x128_f8f6f4 v[146:149], v[26:33], v[206:213], v[146:149], v234, v238 op_sel_hi:[0,0,0]
	v_mfma_scale_f32_16x16x128_f8f6f4 v[142:145], v[18:25], v[216:223], v[142:145], v234, v238 op_sel_hi:[0,0,0]
	v_mfma_scale_f32_16x16x128_f8f6f4 v[138:141], v[26:33], v[216:223], v[138:141], v234, v238 op_sel_hi:[0,0,0]
	v_mfma_scale_f32_16x16x128_f8f6f4 v[134:137], v[18:25], v[224:231], v[134:137], v234, v238 op_sel_hi:[0,0,0]
	v_mfma_scale_f32_16x16x128_f8f6f4 v[130:133], v[26:33], v[224:231], v[130:133], v234, v238 op_sel_hi:[0,0,0]
	s_setprio 0
	s_setprio 1
	v_mfma_scale_f32_16x16x128_f8f6f4 v[126:129], v[2:9], v[198:205], v[126:129], v234, v238 op_sel_hi:[0,0,0]
	v_mfma_scale_f32_16x16x128_f8f6f4 v[122:125], v[10:17], v[198:205], v[122:125], v234, v238 op_sel_hi:[0,0,0]
	v_mfma_scale_f32_16x16x128_f8f6f4 v[118:121], v[2:9], v[206:213], v[118:121], v234, v238 op_sel_hi:[0,0,0]
	v_mfma_scale_f32_16x16x128_f8f6f4 v[114:117], v[10:17], v[206:213], v[114:117], v234, v238 op_sel_hi:[0,0,0]
	v_mfma_scale_f32_16x16x128_f8f6f4 v[110:113], v[2:9], v[216:223], v[110:113], v234, v238 op_sel_hi:[0,0,0]
	v_mfma_scale_f32_16x16x128_f8f6f4 v[106:109], v[10:17], v[216:223], v[106:109], v234, v238 op_sel_hi:[0,0,0]
	v_mfma_scale_f32_16x16x128_f8f6f4 v[102:105], v[2:9], v[224:231], v[102:105], v234, v238 op_sel_hi:[0,0,0]
	v_mfma_scale_f32_16x16x128_f8f6f4 v[98:101], v[10:17], v[224:231], v[98:101], v234, v238 op_sel_hi:[0,0,0]
	s_setprio 0
	s_waitcnt vmcnt(8)
	s_barrier
	s_mov_b64 s[48:49], 0x180
	s_mov_b32 m0, s65
	v_lshl_add_u64 v[172:173], v[172:173], 0, s[48:49]
	s_add_u32 s46, s44, 0x20180
	ds_read_b128 v[198:201], v196 offset:49152
	ds_read_b128 v[202:205], v196 offset:50176
	ds_read_b128 v[206:209], v196 offset:51200
	ds_read_b128 v[210:213], v196 offset:52224
	ds_read_b128 v[216:219], v196 offset:53248
	ds_read_b128 v[220:223], v196 offset:54272
	ds_read_b128 v[224:227], v196 offset:55296
	ds_read_b128 v[228:231], v196 offset:56320
	global_load_lds_dwordx4 v[172:173], off
	v_lshl_add_u64 v[172:173], v[174:175], 0, s[48:49]
	s_mov_b32 m0, s68
	s_addc_u32 s47, s45, 0
	global_load_lds_dwordx4 v[172:173], off
	v_lshl_add_u64 v[172:173], s[46:47], 0, v[0:1]
	s_mov_b32 m0, s51
	s_nop 0
	global_load_lds_dwordx4 v[172:173], off
	v_lshl_add_u64 v[172:173], s[46:47], 0, v[166:167]
	s_mov_b32 m0, s4
	s_nop 0
	global_load_lds_dwordx4 v[172:173], off
	v_lshl_add_u64 v[172:173], v[176:177], 0, s[48:49]
	s_mov_b32 m0, s81
	s_nop 0
	global_load_lds_dwordx4 v[172:173], off
	v_lshl_add_u64 v[172:173], v[178:179], 0, s[48:49]
	s_mov_b32 m0, s50
	s_nop 0
	global_load_lds_dwordx4 v[172:173], off
	s_waitcnt lgkmcnt(0)
	s_barrier
	s_setprio 1
	s_waitcnt lgkmcnt(0)
	v_mfma_scale_f32_16x16x128_f8f6f4 v[94:97], v[18:25], v[198:205], v[94:97], v234, v238 op_sel_hi:[0,0,0]
	v_mfma_scale_f32_16x16x128_f8f6f4 v[90:93], v[26:33], v[198:205], v[90:93], v234, v238 op_sel_hi:[0,0,0]
	v_mfma_scale_f32_16x16x128_f8f6f4 v[86:89], v[18:25], v[206:213], v[86:89], v234, v238 op_sel_hi:[0,0,0]
	v_mfma_scale_f32_16x16x128_f8f6f4 v[82:85], v[26:33], v[206:213], v[82:85], v234, v238 op_sel_hi:[0,0,0]
	v_mfma_scale_f32_16x16x128_f8f6f4 v[78:81], v[18:25], v[216:223], v[78:81], v234, v238 op_sel_hi:[0,0,0]
	v_mfma_scale_f32_16x16x128_f8f6f4 v[74:77], v[26:33], v[216:223], v[74:77], v234, v238 op_sel_hi:[0,0,0]
	v_mfma_scale_f32_16x16x128_f8f6f4 v[70:73], v[18:25], v[224:231], v[70:73], v234, v238 op_sel_hi:[0,0,0]
	v_mfma_scale_f32_16x16x128_f8f6f4 v[66:69], v[26:33], v[224:231], v[66:69], v234, v238 op_sel_hi:[0,0,0]
	s_setprio 0
	s_setprio 1
	v_mfma_scale_f32_16x16x128_f8f6f4 v[62:65], v[2:9], v[198:205], v[62:65], v234, v238 op_sel_hi:[0,0,0]
	v_mfma_scale_f32_16x16x128_f8f6f4 v[58:61], v[10:17], v[198:205], v[58:61], v234, v238 op_sel_hi:[0,0,0]
	v_mfma_scale_f32_16x16x128_f8f6f4 v[54:57], v[2:9], v[206:213], v[54:57], v234, v238 op_sel_hi:[0,0,0]
	v_mfma_scale_f32_16x16x128_f8f6f4 v[50:53], v[10:17], v[206:213], v[50:53], v234, v238 op_sel_hi:[0,0,0]
	v_mfma_scale_f32_16x16x128_f8f6f4 v[46:49], v[2:9], v[216:223], v[46:49], v234, v238 op_sel_hi:[0,0,0]
	v_mfma_scale_f32_16x16x128_f8f6f4 v[42:45], v[10:17], v[216:223], v[42:45], v234, v238 op_sel_hi:[0,0,0]
	v_mfma_scale_f32_16x16x128_f8f6f4 v[38:41], v[2:9], v[224:231], v[38:41], v234, v238 op_sel_hi:[0,0,0]
	v_mfma_scale_f32_16x16x128_f8f6f4 v[34:37], v[10:17], v[224:231], v[34:37], v234, v238 op_sel_hi:[0,0,0]
	s_setprio 0
	s_waitcnt vmcnt(8)
	s_barrier
	s_add_u32 s42, s42, 0x20180
	s_addc_u32 s43, s43, 0
	s_add_u32 s48, s44, 0x200
	s_addc_u32 s49, s45, 0
	s_mov_b32 s74, 0
.Lg2l_BB0_2089:
	ds_read_b128 v[2:5], v180
	ds_read_b128 v[6:9], v181
	ds_read_b128 v[10:13], v182
	ds_read_b128 v[14:17], v183
	ds_read_b128 v[26:29], v184
	ds_read_b128 v[30:33], v185
	ds_read_b128 v[172:175], v186
	ds_read_b128 v[176:179], v187
	s_add_u32 s44, s42, 0xfffe0080
	s_addc_u32 s45, s43, -1
	s_cmp_eq_u32 s74, 4
	s_cselect_b32 s47, s13, s45
	s_cselect_b32 s46, s27, s44
	s_cselect_b32 s45, s35, s49
	s_cselect_b32 s44, s34, s48
	s_mov_b32 m0, s29
	v_lshl_add_u64 v[224:225], s[42:43], 0, v[168:169]
	ds_read_b128 v[18:21], v196
	ds_read_b128 v[22:25], v196 offset:1024
	ds_read_b128 v[198:201], v196 offset:2048
	ds_read_b128 v[202:205], v196 offset:3072
	ds_read_b128 v[206:209], v196 offset:4096
	ds_read_b128 v[210:213], v196 offset:5120
	ds_read_b128 v[216:219], v196 offset:6144
	ds_read_b128 v[220:223], v196 offset:7168
	global_load_lds_dwordx4 v[224:225], off
	v_lshl_add_u64 v[224:225], s[42:43], 0, v[170:171]
	s_mov_b32 m0, s31
	s_nop 0
	global_load_lds_dwordx4 v[224:225], off
	s_waitcnt lgkmcnt(0)
	s_barrier
	s_setprio 1
	s_waitcnt lgkmcnt(0)
	v_mfma_scale_f32_16x16x128_f8f6f4 v[158:161], v[2:9], v[18:25], v[158:161], v234, v238 op_sel_hi:[0,0,0]
	v_mfma_scale_f32_16x16x128_f8f6f4 v[154:157], v[10:17], v[18:25], v[154:157], v234, v238 op_sel_hi:[0,0,0]
	v_mfma_scale_f32_16x16x128_f8f6f4 v[150:153], v[2:9], v[198:205], v[150:153], v234, v238 op_sel_hi:[0,0,0]
	v_mfma_scale_f32_16x16x128_f8f6f4 v[146:149], v[10:17], v[198:205], v[146:149], v234, v238 op_sel_hi:[0,0,0]
	v_mfma_scale_f32_16x16x128_f8f6f4 v[142:145], v[2:9], v[206:213], v[142:145], v234, v238 op_sel_hi:[0,0,0]
	v_mfma_scale_f32_16x16x128_f8f6f4 v[138:141], v[10:17], v[206:213], v[138:141], v234, v238 op_sel_hi:[0,0,0]
	v_mfma_scale_f32_16x16x128_f8f6f4 v[134:137], v[2:9], v[216:223], v[134:137], v234, v238 op_sel_hi:[0,0,0]
	v_mfma_scale_f32_16x16x128_f8f6f4 v[130:133], v[10:17], v[216:223], v[130:133], v234, v238 op_sel_hi:[0,0,0]
	s_setprio 0
	s_setprio 1
	v_mfma_scale_f32_16x16x128_f8f6f4 v[126:129], v[26:33], v[18:25], v[126:129], v234, v238 op_sel_hi:[0,0,0]
	v_mfma_scale_f32_16x16x128_f8f6f4 v[122:125], v[172:179], v[18:25], v[122:125], v234, v238 op_sel_hi:[0,0,0]
	v_mfma_scale_f32_16x16x128_f8f6f4 v[118:121], v[26:33], v[198:205], v[118:121], v234, v238 op_sel_hi:[0,0,0]
	v_mfma_scale_f32_16x16x128_f8f6f4 v[114:117], v[172:179], v[198:205], v[114:117], v234, v238 op_sel_hi:[0,0,0]
	v_mfma_scale_f32_16x16x128_f8f6f4 v[110:113], v[26:33], v[206:213], v[110:113], v234, v238 op_sel_hi:[0,0,0]
	v_mfma_scale_f32_16x16x128_f8f6f4 v[106:109], v[172:179], v[206:213], v[106:109], v234, v238 op_sel_hi:[0,0,0]
	v_mfma_scale_f32_16x16x128_f8f6f4 v[102:105], v[26:33], v[216:223], v[102:105], v234, v238 op_sel_hi:[0,0,0]
	v_mfma_scale_f32_16x16x128_f8f6f4 v[98:101], v[172:179], v[216:223], v[98:101], v234, v238 op_sel_hi:[0,0,0]
	s_setprio 0
	s_waitcnt vmcnt(8)
	s_barrier
	s_mov_b32 m0, s41
	v_lshl_add_u64 v[18:19], s[44:45], 0, v[0:1]
	s_add_u32 vcc_lo, s44, 0x20000
	ds_read_b128 v[198:201], v196 offset:16384
	ds_read_b128 v[202:205], v196 offset:17408
	ds_read_b128 v[206:209], v196 offset:18432
	ds_read_b128 v[210:213], v196 offset:19456
	ds_read_b128 v[216:219], v196 offset:20480
	ds_read_b128 v[220:223], v196 offset:21504
	ds_read_b128 v[224:227], v196 offset:22528
	ds_read_b128 v[228:231], v196 offset:23552
	global_load_lds_dwordx4 v[18:19], off
	v_lshl_add_u64 v[20:21], s[44:45], 0, v[166:167]
	s_mov_b32 m0, s57
	s_addc_u32 vcc_hi, s45, 0
	global_load_lds_dwordx4 v[20:21], off
	v_lshl_add_u64 v[22:23], vcc, 0, v[0:1]
	s_mov_b32 m0, s58
	v_lshl_add_u64 v[24:25], s[46:47], 0, v[164:165]
	global_load_lds_dwordx4 v[22:23], off
	v_lshl_add_u64 v[22:23], vcc, 0, v[166:167]
	s_mov_b32 m0, s59
	s_nop 0
	global_load_lds_dwordx4 v[22:23], off
	v_lshl_add_u64 v[22:23], s[46:47], 0, v[162:163]
	s_mov_b32 m0, s37
	s_nop 0
	global_load_lds_dwordx4 v[22:23], off
	s_mov_b32 m0, s60
	s_nop 0
	global_load_lds_dwordx4 v[24:25], off
	s_waitcnt lgkmcnt(0)
	s_barrier
	s_setprio 1
	s_waitcnt lgkmcnt(0)
	v_mfma_scale_f32_16x16x128_f8f6f4 v[94:97], v[2:9], v[198:205], v[94:97], v234, v238 op_sel_hi:[0,0,0]
	v_mfma_scale_f32_16x16x128_f8f6f4 v[90:93], v[10:17], v[198:205], v[90:93], v234, v238 op_sel_hi:[0,0,0]
	v_mfma_scale_f32_16x16x128_f8f6f4 v[86:89], v[2:9], v[206:213], v[86:89], v234, v238 op_sel_hi:[0,0,0]
	v_mfma_scale_f32_16x16x128_f8f6f4 v[82:85], v[10:17], v[206:213], v[82:85], v234, v238 op_sel_hi:[0,0,0]
	v_mfma_scale_f32_16x16x128_f8f6f4 v[78:81], v[2:9], v[216:223], v[78:81], v234, v238 op_sel_hi:[0,0,0]
	v_mfma_scale_f32_16x16x128_f8f6f4 v[74:77], v[10:17], v[216:223], v[74:77], v234, v238 op_sel_hi:[0,0,0]
	v_mfma_scale_f32_16x16x128_f8f6f4 v[70:73], v[2:9], v[224:231], v[70:73], v234, v238 op_sel_hi:[0,0,0]
	v_mfma_scale_f32_16x16x128_f8f6f4 v[66:69], v[10:17], v[224:231], v[66:69], v234, v238 op_sel_hi:[0,0,0]
	s_setprio 0
	s_setprio 1
	v_mfma_scale_f32_16x16x128_f8f6f4 v[62:65], v[26:33], v[198:205], v[62:65], v234, v238 op_sel_hi:[0,0,0]
	v_mfma_scale_f32_16x16x128_f8f6f4 v[58:61], v[172:179], v[198:205], v[58:61], v234, v238 op_sel_hi:[0,0,0]
	v_mfma_scale_f32_16x16x128_f8f6f4 v[54:57], v[26:33], v[206:213], v[54:57], v234, v238 op_sel_hi:[0,0,0]
	v_mfma_scale_f32_16x16x128_f8f6f4 v[50:53], v[172:179], v[206:213], v[50:53], v234, v238 op_sel_hi:[0,0,0]
	v_mfma_scale_f32_16x16x128_f8f6f4 v[46:49], v[26:33], v[216:223], v[46:49], v234, v238 op_sel_hi:[0,0,0]
	v_mfma_scale_f32_16x16x128_f8f6f4 v[42:45], v[172:179], v[216:223], v[42:45], v234, v238 op_sel_hi:[0,0,0]
	v_mfma_scale_f32_16x16x128_f8f6f4 v[38:41], v[26:33], v[224:231], v[38:41], v234, v238 op_sel_hi:[0,0,0]
	v_mfma_scale_f32_16x16x128_f8f6f4 v[34:37], v[172:179], v[224:231], v[34:37], v234, v238 op_sel_hi:[0,0,0]
	s_setprio 0
	s_waitcnt vmcnt(8)
	s_barrier
	ds_read_b128 v[10:13], v188
	ds_read_b128 v[14:17], v189
	ds_read_b128 v[26:29], v190
	ds_read_b128 v[30:33], v191
	ds_read_b128 v[2:5], v192
	ds_read_b128 v[6:9], v193
	ds_read_b128 v[172:175], v194
	ds_read_b128 v[176:179], v195
	s_add_u32 s46, s46, 0x20000
	s_addc_u32 s47, s47, 0
	s_mov_b32 m0, s61
	v_lshl_add_u64 v[232:233], s[46:47], 0, v[162:163]
	ds_read_b128 v[198:201], v196 offset:32768
	ds_read_b128 v[202:205], v196 offset:33792
	ds_read_b128 v[206:209], v196 offset:34816
	ds_read_b128 v[210:213], v196 offset:35840
	ds_read_b128 v[216:219], v196 offset:36864
	ds_read_b128 v[220:223], v196 offset:37888
	ds_read_b128 v[224:227], v196 offset:38912
	ds_read_b128 v[228:231], v196 offset:39936
	global_load_lds_dwordx4 v[232:233], off
	v_lshl_add_u64 v[232:233], s[46:47], 0, v[164:165]
	s_mov_b32 m0, s62
	s_nop 0
	global_load_lds_dwordx4 v[232:233], off
	s_waitcnt lgkmcnt(0)
	s_barrier
	s_setprio 1
	s_waitcnt lgkmcnt(0)
	v_mfma_scale_f32_16x16x128_f8f6f4 v[158:161], v[10:17], v[198:205], v[158:161], v234, v238 op_sel_hi:[0,0,0]
	v_mfma_scale_f32_16x16x128_f8f6f4 v[154:157], v[26:33], v[198:205], v[154:157], v234, v238 op_sel_hi:[0,0,0]
	v_mfma_scale_f32_16x16x128_f8f6f4 v[150:153], v[10:17], v[206:213], v[150:153], v234, v238 op_sel_hi:[0,0,0]
	v_mfma_scale_f32_16x16x128_f8f6f4 v[146:149], v[26:33], v[206:213], v[146:149], v234, v238 op_sel_hi:[0,0,0]
	v_mfma_scale_f32_16x16x128_f8f6f4 v[142:145], v[10:17], v[216:223], v[142:145], v234, v238 op_sel_hi:[0,0,0]
	v_mfma_scale_f32_16x16x128_f8f6f4 v[138:141], v[26:33], v[216:223], v[138:141], v234, v238 op_sel_hi:[0,0,0]
	v_mfma_scale_f32_16x16x128_f8f6f4 v[134:137], v[10:17], v[224:231], v[134:137], v234, v238 op_sel_hi:[0,0,0]
	v_mfma_scale_f32_16x16x128_f8f6f4 v[130:133], v[26:33], v[224:231], v[130:133], v234, v238 op_sel_hi:[0,0,0]
	s_setprio 0
	s_setprio 1
	v_mfma_scale_f32_16x16x128_f8f6f4 v[126:129], v[2:9], v[198:205], v[126:129], v234, v238 op_sel_hi:[0,0,0]
	v_mfma_scale_f32_16x16x128_f8f6f4 v[122:125], v[172:179], v[198:205], v[122:125], v234, v238 op_sel_hi:[0,0,0]
	v_mfma_scale_f32_16x16x128_f8f6f4 v[118:121], v[2:9], v[206:213], v[118:121], v234, v238 op_sel_hi:[0,0,0]
	v_mfma_scale_f32_16x16x128_f8f6f4 v[114:117], v[172:179], v[206:213], v[114:117], v234, v238 op_sel_hi:[0,0,0]
	v_mfma_scale_f32_16x16x128_f8f6f4 v[110:113], v[2:9], v[216:223], v[110:113], v234, v238 op_sel_hi:[0,0,0]
	v_mfma_scale_f32_16x16x128_f8f6f4 v[106:109], v[172:179], v[216:223], v[106:109], v234, v238 op_sel_hi:[0,0,0]
	v_mfma_scale_f32_16x16x128_f8f6f4 v[102:105], v[2:9], v[224:231], v[102:105], v234, v238 op_sel_hi:[0,0,0]
	v_mfma_scale_f32_16x16x128_f8f6f4 v[98:101], v[172:179], v[224:231], v[98:101], v234, v238 op_sel_hi:[0,0,0]
	s_setprio 0
	s_waitcnt vmcnt(8)
	s_barrier
	s_mov_b32 m0, s65
	v_lshl_add_u64 v[18:19], v[18:19], 0, s[66:67]
	s_add_u32 s44, s44, 0x20080
	ds_read_b128 v[198:201], v196 offset:49152
	ds_read_b128 v[202:205], v196 offset:50176
	ds_read_b128 v[206:209], v196 offset:51200
	ds_read_b128 v[210:213], v196 offset:52224
	ds_read_b128 v[216:219], v196 offset:53248
	ds_read_b128 v[220:223], v196 offset:54272
	ds_read_b128 v[224:227], v196 offset:55296
	ds_read_b128 v[228:231], v196 offset:56320
	global_load_lds_dwordx4 v[18:19], off
	v_lshl_add_u64 v[18:19], v[20:21], 0, s[66:67]
	s_mov_b32 m0, s68
	s_addc_u32 s45, s45, 0
	global_load_lds_dwordx4 v[18:19], off
	v_lshl_add_u64 v[18:19], s[44:45], 0, v[0:1]
	s_mov_b32 m0, s51
	s_nop 0
	global_load_lds_dwordx4 v[18:19], off
	v_lshl_add_u64 v[18:19], s[44:45], 0, v[166:167]
	s_mov_b32 m0, s4
	s_nop 0
	global_load_lds_dwordx4 v[18:19], off
	v_lshl_add_u64 v[18:19], v[22:23], 0, s[66:67]
	s_mov_b32 m0, s81
	s_nop 0
	global_load_lds_dwordx4 v[18:19], off
	v_lshl_add_u64 v[18:19], v[24:25], 0, s[66:67]
	s_mov_b32 m0, s50
	s_nop 0
	global_load_lds_dwordx4 v[18:19], off
	s_waitcnt lgkmcnt(0)
	s_barrier
	s_setprio 1
	s_waitcnt lgkmcnt(0)
	v_mfma_scale_f32_16x16x128_f8f6f4 v[94:97], v[10:17], v[198:205], v[94:97], v234, v238 op_sel_hi:[0,0,0]
	v_mfma_scale_f32_16x16x128_f8f6f4 v[90:93], v[26:33], v[198:205], v[90:93], v234, v238 op_sel_hi:[0,0,0]
	v_mfma_scale_f32_16x16x128_f8f6f4 v[86:89], v[10:17], v[206:213], v[86:89], v234, v238 op_sel_hi:[0,0,0]
	v_mfma_scale_f32_16x16x128_f8f6f4 v[82:85], v[26:33], v[206:213], v[82:85], v234, v238 op_sel_hi:[0,0,0]
	v_mfma_scale_f32_16x16x128_f8f6f4 v[78:81], v[10:17], v[216:223], v[78:81], v234, v238 op_sel_hi:[0,0,0]
	v_mfma_scale_f32_16x16x128_f8f6f4 v[74:77], v[26:33], v[216:223], v[74:77], v234, v238 op_sel_hi:[0,0,0]
	v_mfma_scale_f32_16x16x128_f8f6f4 v[70:73], v[10:17], v[224:231], v[70:73], v234, v238 op_sel_hi:[0,0,0]
	v_mfma_scale_f32_16x16x128_f8f6f4 v[66:69], v[26:33], v[224:231], v[66:69], v234, v238 op_sel_hi:[0,0,0]
	s_setprio 0
	s_setprio 1
	v_mfma_scale_f32_16x16x128_f8f6f4 v[62:65], v[2:9], v[198:205], v[62:65], v234, v238 op_sel_hi:[0,0,0]
	v_mfma_scale_f32_16x16x128_f8f6f4 v[58:61], v[172:179], v[198:205], v[58:61], v234, v238 op_sel_hi:[0,0,0]
	v_mfma_scale_f32_16x16x128_f8f6f4 v[54:57], v[2:9], v[206:213], v[54:57], v234, v238 op_sel_hi:[0,0,0]
	v_mfma_scale_f32_16x16x128_f8f6f4 v[50:53], v[172:179], v[206:213], v[50:53], v234, v238 op_sel_hi:[0,0,0]
	v_mfma_scale_f32_16x16x128_f8f6f4 v[46:49], v[2:9], v[216:223], v[46:49], v234, v238 op_sel_hi:[0,0,0]
	v_mfma_scale_f32_16x16x128_f8f6f4 v[42:45], v[172:179], v[216:223], v[42:45], v234, v238 op_sel_hi:[0,0,0]
	v_mfma_scale_f32_16x16x128_f8f6f4 v[38:41], v[2:9], v[224:231], v[38:41], v234, v238 op_sel_hi:[0,0,0]
	v_mfma_scale_f32_16x16x128_f8f6f4 v[34:37], v[172:179], v[224:231], v[34:37], v234, v238 op_sel_hi:[0,0,0]
	s_setprio 0
	s_waitcnt vmcnt(8)
	s_barrier
	s_add_i32 s74, s74, 2
	s_add_u32 s42, s42, 0x100
	s_addc_u32 s43, s43, 0
	s_add_u32 s48, s48, 0x100
	s_addc_u32 s49, s49, 0
	s_cmp_gt_u32 s74, 5
	s_cbranch_scc0 .Lg2l_BB0_2089
.Lg2_join:
	s_and_b64 vcc, exec, s[8:9]
	s_cbranch_vccz .LBB0_2092
	s_barrier
.LBB0_2092:
	s_lshl_b32 s13, s26, 10
	v_mbcnt_lo_u32_b32 v6, -1, 0
	v_mbcnt_hi_u32_b32 v6, -1, v6
	s_and_b32 s13, s13, 0x400
	v_ashrrev_i32_e32 v2, 1, v6
	v_and_b32_e32 v27, -8, v2
	s_add_i32 s13, s5, s13
	v_lshl_add_u32 v12, v27, 2, s13
	ds_read_b128 v[2:5], v12
	ds_read_b128 v[8:11], v12 offset:16
	ds_read_b128 v[18:21], v12 offset:512
	ds_read_b128 v[22:25], v12 offset:528
	s_lshl_b32 s13, s40, 8
	s_add_i32 s13, s13, s63
	s_waitcnt lgkmcnt(0)
	v_pk_mul_f32 v[14:15], v[2:3], s[22:23] op_sel_hi:[1,0]
	v_pk_mul_f32 v[16:17], v[8:9], s[22:23] op_sel_hi:[1,0]
	v_and_or_b32 v26, v6, 15, s13
	v_pk_mul_f32 v[6:7], v[4:5], s[22:23] op_sel_hi:[1,0]
	v_pk_mul_f32 v[12:13], v[10:11], s[22:23] op_sel_hi:[1,0]
	v_pk_mul_f32 v[4:5], v[24:25], s[22:23] op_sel_hi:[1,0]
	v_pk_mul_f32 v[10:11], v[22:23], s[22:23] op_sel_hi:[1,0]
	v_pk_fma_f32 v[22:23], v[158:159], s[22:23], v[14:15] op_sel_hi:[1,0,1]
	v_pk_fma_f32 v[24:25], v[154:155], s[22:23], v[16:17] op_sel_hi:[1,0,1]
	v_mov_b32_e32 v28, v1
	v_mov_b32_e32 v29, v1
	v_cvt_pk_fp8_f32 v28, v22, v23
	v_cvt_pk_fp8_f32 v29, v24, v25
	v_pk_mul_f32 v[8:9], v[18:19], s[22:23] op_sel_hi:[1,0]
	v_pk_fma_f32 v[22:23], v[160:161], s[22:23], v[6:7] op_sel_hi:[1,0,1]
	v_pk_fma_f32 v[24:25], v[156:157], s[22:23], v[12:13] op_sel_hi:[1,0,1]
	v_cvt_pk_fp8_f32 v28, v22, v23 op_sel:[0,0,1]
	v_cvt_pk_fp8_f32 v29, v24, v25 op_sel:[0,0,1]
	v_pk_fma_f32 v[22:23], v[126:127], s[22:23], v[8:9] op_sel_hi:[1,0,1]
	v_pk_fma_f32 v[24:25], v[122:123], s[22:23], v[10:11] op_sel_hi:[1,0,1]
	v_mov_b32_e32 v30, v1
	v_mov_b32_e32 v31, v1
	v_cvt_pk_fp8_f32 v30, v22, v23
	v_cvt_pk_fp8_f32 v31, v24, v25
	s_lshl_b32 s13, s36, 8
	v_pk_mul_f32 v[2:3], v[20:21], s[22:23] op_sel_hi:[1,0]
	s_or_b32 s13, s13, s64
	v_add_u32_e32 v20, s13, v27
	v_ashrrev_i32_e32 v27, 31, v26
	v_pk_fma_f32 v[22:23], v[128:129], s[22:23], v[2:3] op_sel_hi:[1,0,1]
	v_pk_fma_f32 v[24:25], v[124:125], s[22:23], v[4:5] op_sel_hi:[1,0,1]
	v_lshlrev_b64 v[18:19], 10, v[26:27]
	v_cvt_pk_fp8_f32 v30, v22, v23 op_sel:[0,0,1]
	v_cvt_pk_fp8_f32 v31, v24, v25 op_sel:[0,0,1]
	v_ashrrev_i32_e32 v21, 31, v20
	v_lshl_add_u64 v[18:19], s[6:7], 0, v[18:19]
	v_lshl_add_u64 v[18:19], v[18:19], 0, v[20:21]
	global_store_dwordx2 v[18:19], v[28:29], off
	global_store_dwordx2 v[18:19], v[30:31], off offset:128
	v_pk_fma_f32 v[24:25], v[150:151], s[22:23], v[14:15] op_sel_hi:[1,0,1]
	v_pk_fma_f32 v[28:29], v[146:147], s[22:23], v[16:17] op_sel_hi:[1,0,1]
	v_mov_b32_e32 v30, v1
	v_mov_b32_e32 v31, v1
	v_cvt_pk_fp8_f32 v30, v24, v25
	v_cvt_pk_fp8_f32 v31, v28, v29
	v_pk_fma_f32 v[24:25], v[152:153], s[22:23], v[6:7] op_sel_hi:[1,0,1]
	v_pk_fma_f32 v[28:29], v[148:149], s[22:23], v[12:13] op_sel_hi:[1,0,1]
	v_cvt_pk_fp8_f32 v30, v24, v25 op_sel:[0,0,1]
	v_cvt_pk_fp8_f32 v31, v28, v29 op_sel:[0,0,1]
	v_pk_fma_f32 v[24:25], v[118:119], s[22:23], v[8:9] op_sel_hi:[1,0,1]
	v_pk_fma_f32 v[28:29], v[114:115], s[22:23], v[10:11] op_sel_hi:[1,0,1]
	v_mov_b32_e32 v32, v1
	v_mov_b32_e32 v33, v1
	v_cvt_pk_fp8_f32 v32, v24, v25
	v_cvt_pk_fp8_f32 v33, v28, v29
	v_or_b32_e32 v22, 16, v26
	v_ashrrev_i32_e32 v23, 31, v22
	v_pk_fma_f32 v[24:25], v[120:121], s[22:23], v[2:3] op_sel_hi:[1,0,1]
	v_pk_fma_f32 v[28:29], v[116:117], s[22:23], v[4:5] op_sel_hi:[1,0,1]
	v_lshlrev_b64 v[22:23], 10, v[22:23]
	v_cvt_pk_fp8_f32 v32, v24, v25 op_sel:[0,0,1]
	v_cvt_pk_fp8_f32 v33, v28, v29 op_sel:[0,0,1]
	v_lshl_add_u64 v[22:23], s[6:7], 0, v[22:23]
	v_lshl_add_u64 v[22:23], v[22:23], 0, v[20:21]
	global_store_dwordx2 v[22:23], v[30:31], off
	global_store_dwordx2 v[22:23], v[32:33], off offset:128
	v_pk_fma_f32 v[24:25], v[142:143], s[22:23], v[14:15] op_sel_hi:[1,0,1]
	v_pk_fma_f32 v[28:29], v[138:139], s[22:23], v[16:17] op_sel_hi:[1,0,1]
	v_mov_b32_e32 v30, v1
	v_mov_b32_e32 v31, v1
	v_cvt_pk_fp8_f32 v30, v24, v25
	v_cvt_pk_fp8_f32 v31, v28, v29
	v_pk_fma_f32 v[24:25], v[144:145], s[22:23], v[6:7] op_sel_hi:[1,0,1]
	v_pk_fma_f32 v[28:29], v[140:141], s[22:23], v[12:13] op_sel_hi:[1,0,1]
	v_cvt_pk_fp8_f32 v30, v24, v25 op_sel:[0,0,1]
	v_cvt_pk_fp8_f32 v31, v28, v29 op_sel:[0,0,1]
	v_pk_fma_f32 v[24:25], v[110:111], s[22:23], v[8:9] op_sel_hi:[1,0,1]
	v_pk_fma_f32 v[28:29], v[106:107], s[22:23], v[10:11] op_sel_hi:[1,0,1]
	v_mov_b32_e32 v32, v1
	v_mov_b32_e32 v33, v1
	v_cvt_pk_fp8_f32 v32, v24, v25
	v_cvt_pk_fp8_f32 v33, v28, v29
	v_or_b32_e32 v22, 32, v26
	v_ashrrev_i32_e32 v23, 31, v22
	v_pk_fma_f32 v[24:25], v[112:113], s[22:23], v[2:3] op_sel_hi:[1,0,1]
	v_pk_fma_f32 v[28:29], v[108:109], s[22:23], v[4:5] op_sel_hi:[1,0,1]
	v_lshlrev_b64 v[22:23], 10, v[22:23]
	v_cvt_pk_fp8_f32 v32, v24, v25 op_sel:[0,0,1]
	v_cvt_pk_fp8_f32 v33, v28, v29 op_sel:[0,0,1]
	v_lshl_add_u64 v[22:23], s[6:7], 0, v[22:23]
	v_lshl_add_u64 v[22:23], v[22:23], 0, v[20:21]
	global_store_dwordx2 v[22:23], v[30:31], off
	global_store_dwordx2 v[22:23], v[32:33], off offset:128
	v_or_b32_e32 v22, 48, v26
	v_pk_fma_f32 v[24:25], v[134:135], s[22:23], v[14:15] op_sel_hi:[1,0,1]
	v_pk_fma_f32 v[26:27], v[130:131], s[22:23], v[16:17] op_sel_hi:[1,0,1]
	v_mov_b32_e32 v28, v1
	v_mov_b32_e32 v29, v1
	v_cvt_pk_fp8_f32 v28, v24, v25
	v_cvt_pk_fp8_f32 v29, v26, v27
	v_pk_fma_f32 v[24:25], v[136:137], s[22:23], v[6:7] op_sel_hi:[1,0,1]
	v_pk_fma_f32 v[26:27], v[132:133], s[22:23], v[12:13] op_sel_hi:[1,0,1]
	v_cvt_pk_fp8_f32 v28, v24, v25 op_sel:[0,0,1]
	v_cvt_pk_fp8_f32 v29, v26, v27 op_sel:[0,0,1]
	v_pk_fma_f32 v[24:25], v[102:103], s[22:23], v[8:9] op_sel_hi:[1,0,1]
	v_pk_fma_f32 v[26:27], v[98:99], s[22:23], v[10:11] op_sel_hi:[1,0,1]
	v_mov_b32_e32 v30, v1
	v_mov_b32_e32 v31, v1
	v_cvt_pk_fp8_f32 v30, v24, v25
	v_cvt_pk_fp8_f32 v31, v26, v27
	v_ashrrev_i32_e32 v23, 31, v22
	v_lshlrev_b64 v[22:23], 10, v[22:23]
	v_pk_fma_f32 v[24:25], v[104:105], s[22:23], v[2:3] op_sel_hi:[1,0,1]
	v_pk_fma_f32 v[26:27], v[100:101], s[22:23], v[4:5] op_sel_hi:[1,0,1]
	v_lshl_add_u64 v[22:23], s[6:7], 0, v[22:23]
	v_cvt_pk_fp8_f32 v30, v24, v25 op_sel:[0,0,1]
	v_cvt_pk_fp8_f32 v31, v26, v27 op_sel:[0,0,1]
	v_lshl_add_u64 v[20:21], v[22:23], 0, v[20:21]
	v_pk_fma_f32 v[22:23], v[94:95], s[22:23], v[14:15] op_sel_hi:[1,0,1]
	v_pk_fma_f32 v[24:25], v[90:91], s[22:23], v[16:17] op_sel_hi:[1,0,1]
	v_mov_b32_e32 v26, v1
	v_mov_b32_e32 v27, v1
	v_cvt_pk_fp8_f32 v26, v22, v23
	v_cvt_pk_fp8_f32 v27, v24, v25
	v_pk_fma_f32 v[22:23], v[96:97], s[22:23], v[6:7] op_sel_hi:[1,0,1]
	v_pk_fma_f32 v[24:25], v[92:93], s[22:23], v[12:13] op_sel_hi:[1,0,1]
	global_store_dwordx2 v[20:21], v[28:29], off
	global_store_dwordx2 v[20:21], v[30:31], off offset:128
	v_cvt_pk_fp8_f32 v26, v22, v23 op_sel:[0,0,1]
	v_cvt_pk_fp8_f32 v27, v24, v25 op_sel:[0,0,1]
	v_pk_fma_f32 v[22:23], v[62:63], s[22:23], v[8:9] op_sel_hi:[1,0,1]
	v_pk_fma_f32 v[24:25], v[58:59], s[22:23], v[10:11] op_sel_hi:[1,0,1]
	v_mov_b32_e32 v28, v1
	v_mov_b32_e32 v29, v1
	v_cvt_pk_fp8_f32 v28, v22, v23
	v_cvt_pk_fp8_f32 v29, v24, v25
	v_pk_fma_f32 v[22:23], v[64:65], s[22:23], v[2:3] op_sel_hi:[1,0,1]
	v_pk_fma_f32 v[24:25], v[60:61], s[22:23], v[4:5] op_sel_hi:[1,0,1]
	v_cvt_pk_fp8_f32 v28, v22, v23 op_sel:[0,0,1]
	v_cvt_pk_fp8_f32 v29, v24, v25 op_sel:[0,0,1]
	s_mov_b32 s13, 0x20000
	v_add_co_u32_e32 v22, vcc, s13, v18
	s_mov_b64 s[26:27], 0x20000
	s_nop 0
	v_addc_co_u32_e32 v23, vcc, 0, v19, vcc
	v_lshl_add_u64 v[20:21], v[18:19], 0, s[26:27]
	global_store_dwordx2 v[22:23], v[26:27], off
	global_store_dwordx2 v[20:21], v[28:29], off offset:128
	v_pk_fma_f32 v[22:23], v[86:87], s[22:23], v[14:15] op_sel_hi:[1,0,1]
	v_pk_fma_f32 v[24:25], v[82:83], s[22:23], v[16:17] op_sel_hi:[1,0,1]
	v_mov_b32_e32 v26, v1
	v_mov_b32_e32 v27, v1
	v_cvt_pk_fp8_f32 v26, v22, v23
	v_cvt_pk_fp8_f32 v27, v24, v25
	v_pk_fma_f32 v[22:23], v[88:89], s[22:23], v[6:7] op_sel_hi:[1,0,1]
	v_pk_fma_f32 v[24:25], v[84:85], s[22:23], v[12:13] op_sel_hi:[1,0,1]
	v_cvt_pk_fp8_f32 v26, v22, v23 op_sel:[0,0,1]
	v_cvt_pk_fp8_f32 v27, v24, v25 op_sel:[0,0,1]
	v_pk_fma_f32 v[22:23], v[54:55], s[22:23], v[8:9] op_sel_hi:[1,0,1]
	v_pk_fma_f32 v[24:25], v[50:51], s[22:23], v[10:11] op_sel_hi:[1,0,1]
	v_mov_b32_e32 v28, v1
	v_mov_b32_e32 v29, v1
	v_cvt_pk_fp8_f32 v28, v22, v23
	v_cvt_pk_fp8_f32 v29, v24, v25
	v_pk_fma_f32 v[22:23], v[56:57], s[22:23], v[2:3] op_sel_hi:[1,0,1]
	v_pk_fma_f32 v[24:25], v[52:53], s[22:23], v[4:5] op_sel_hi:[1,0,1]
	v_cvt_pk_fp8_f32 v28, v22, v23 op_sel:[0,0,1]
	v_cvt_pk_fp8_f32 v29, v24, v25 op_sel:[0,0,1]
	s_mov_b32 s13, 0x24000
	v_add_co_u32_e32 v22, vcc, s13, v18
	s_mov_b64 s[26:27], 0x24000
	s_nop 0
	v_addc_co_u32_e32 v23, vcc, 0, v19, vcc
	v_lshl_add_u64 v[20:21], v[18:19], 0, s[26:27]
	global_store_dwordx2 v[22:23], v[26:27], off
	global_store_dwordx2 v[20:21], v[28:29], off offset:128
	v_pk_fma_f32 v[22:23], v[78:79], s[22:23], v[14:15] op_sel_hi:[1,0,1]
	v_pk_fma_f32 v[24:25], v[74:75], s[22:23], v[16:17] op_sel_hi:[1,0,1]
	v_mov_b32_e32 v26, v1
	v_mov_b32_e32 v27, v1
	v_cvt_pk_fp8_f32 v26, v22, v23
	v_cvt_pk_fp8_f32 v27, v24, v25
	v_pk_fma_f32 v[22:23], v[80:81], s[22:23], v[6:7] op_sel_hi:[1,0,1]
	v_pk_fma_f32 v[24:25], v[76:77], s[22:23], v[12:13] op_sel_hi:[1,0,1]
	v_cvt_pk_fp8_f32 v26, v22, v23 op_sel:[0,0,1]
	v_cvt_pk_fp8_f32 v27, v24, v25 op_sel:[0,0,1]
	v_pk_fma_f32 v[22:23], v[46:47], s[22:23], v[8:9] op_sel_hi:[1,0,1]
	v_pk_fma_f32 v[24:25], v[42:43], s[22:23], v[10:11] op_sel_hi:[1,0,1]
	v_mov_b32_e32 v28, v1
	v_mov_b32_e32 v29, v1
	v_cvt_pk_fp8_f32 v28, v22, v23
	v_cvt_pk_fp8_f32 v29, v24, v25
	v_pk_fma_f32 v[22:23], v[48:49], s[22:23], v[2:3] op_sel_hi:[1,0,1]
	v_pk_fma_f32 v[24:25], v[44:45], s[22:23], v[4:5] op_sel_hi:[1,0,1]
	v_cvt_pk_fp8_f32 v28, v22, v23 op_sel:[0,0,1]
	v_cvt_pk_fp8_f32 v29, v24, v25 op_sel:[0,0,1]
	s_mov_b32 s13, 0x28000
	v_add_co_u32_e32 v22, vcc, s13, v18
	s_mov_b64 s[26:27], 0x28000
	s_nop 0
	v_addc_co_u32_e32 v23, vcc, 0, v19, vcc
	v_lshl_add_u64 v[20:21], v[18:19], 0, s[26:27]
	global_store_dwordx2 v[22:23], v[26:27], off
	global_store_dwordx2 v[20:21], v[28:29], off offset:128
	v_pk_fma_f32 v[14:15], v[70:71], s[22:23], v[14:15] op_sel_hi:[1,0,1]
	v_mov_b32_e32 v22, v1
	v_cvt_pk_fp8_f32 v22, v14, v15
	v_pk_fma_f32 v[16:17], v[66:67], s[22:23], v[16:17] op_sel_hi:[1,0,1]
	v_mov_b32_e32 v23, v1
	v_pk_fma_f32 v[6:7], v[72:73], s[22:23], v[6:7] op_sel_hi:[1,0,1]
	v_cvt_pk_fp8_f32 v23, v16, v17
	v_cvt_pk_fp8_f32 v22, v6, v7 op_sel:[0,0,1]
	v_pk_fma_f32 v[6:7], v[38:39], s[22:23], v[8:9] op_sel_hi:[1,0,1]
	v_pk_fma_f32 v[8:9], v[34:35], s[22:23], v[10:11] op_sel_hi:[1,0,1]
	v_mov_b32_e32 v10, v1
	v_mov_b32_e32 v11, v1
	v_cvt_pk_fp8_f32 v10, v6, v7
	v_cvt_pk_fp8_f32 v11, v8, v9
	v_pk_fma_f32 v[12:13], v[68:69], s[22:23], v[12:13] op_sel_hi:[1,0,1]
	v_pk_fma_f32 v[2:3], v[40:41], s[22:23], v[2:3] op_sel_hi:[1,0,1]
	v_cvt_pk_fp8_f32 v23, v12, v13 op_sel:[0,0,1]
	v_pk_fma_f32 v[4:5], v[36:37], s[22:23], v[4:5] op_sel_hi:[1,0,1]
	s_mov_b32 s13, 0x2c000
	v_cvt_pk_fp8_f32 v10, v2, v3 op_sel:[0,0,1]
	v_cvt_pk_fp8_f32 v11, v4, v5 op_sel:[0,0,1]
	v_add_co_u32_e32 v2, vcc, s13, v18
	s_mov_b64 s[26:27], 0x2c000
	s_nop 0
	v_addc_co_u32_e32 v3, vcc, 0, v19, vcc
	s_and_b64 vcc, exec, s[0:1]
	s_mov_b64 s[0:1], -1
	v_lshl_add_u64 v[20:21], v[18:19], 0, s[26:27]
	global_store_dwordx2 v[2:3], v[22:23], off
	global_store_dwordx2 v[20:21], v[10:11], off offset:128
	s_cbranch_vccnz .LBB0_2075
	v_readlane_b32 s0, v254, 40
	v_readlane_b32 s1, v254, 41
	s_andn2_b64 vcc, exec, s[0:1]
	s_cbranch_vccnz .LBB0_2074
	s_barrier
	s_branch .LBB0_2074
